# speedup vs baseline: 1.0539x; 1.0013x over previous
.Lq_spin_0:
	s_sleep 2
	ds_read_b32 v9, v7 offset:0
	s_waitcnt lgkmcnt(0)
	v_cmp_eq_u32_e32 vcc, 0, v9
	s_cbranch_vccnz .Lq_spin_0

.Lq_spin_1:
	s_sleep 2
	ds_read_b32 v9, v7 offset:32
	s_waitcnt lgkmcnt(0)
	v_cmp_eq_u32_e32 vcc, 0, v9
	s_cbranch_vccnz .Lq_spin_1

.Lq_spin_2:
	s_sleep 2
	ds_read_b32 v9, v7 offset:64
	s_waitcnt lgkmcnt(0)
	v_cmp_eq_u32_e32 vcc, 0, v9
	s_cbranch_vccnz .Lq_spin_2

.Lq_spin_3:
	s_sleep 2
	ds_read_b32 v9, v7 offset:96
	s_waitcnt lgkmcnt(0)
	v_cmp_eq_u32_e32 vcc, 0, v9
	s_cbranch_vccnz .Lq_spin_3
